# v39 + GEMM2: the 64 clamps of the ai=0 accumulators done in place between the fourth-phase MFMAs (4 per MFMA) instead of in the serial epilogue
# speedup vs baseline: 1.0127x; 1.0004x over previous
; #define PG8_STAGE(bufoff, gbase, voff) do { _Pragma("unroll") for (int _i = 0; _i < 2; ++_i) \
;         __builtin_amdgcn_global_load_lds((const unsigned*)((const char*)(gbase) + (voff)[_i]), (LAS unsigned*)(lds + (bufoff) + ldsw + _i * 8192), 16, 0, 0); } while (0)
; #define PG8_LDA(dst, b, h) do { _Pragma("unroll") for (int m = 0; m < 4; ++m) _Pragma("unroll") for (int k = 0; k < 2; ++k) dst[m][k] = *(const LAS bf16x8*)(lds + PG8_SA(b, h) + aoff + m * 2048 + k * 1024); } while (0)
; #define PG8_LDB(dst, b, h) do { _Pragma("unroll") for (int n = 0; n < 2; ++n) _Pragma("unroll") for (int k = 0; k < 2; ++k) dst[n][k] = *(const LAS bf16x8*)(lds + PG8_SB(b, h) + boff + n * 2048 + k * 1024); } while (0)
; #define PG8_WAIT_V(n) asm volatile("s_waitcnt vmcnt(" #n ")" ::: "memory")
; #define PG8_WAIT_L(n) asm volatile("s_waitcnt lgkmcnt(" #n ")" ::: "memory")
; #define PG8_BAR __builtin_amdgcn_s_barrier()
; #define PG8_SCHED __builtin_amdgcn_sched_barrier(0)
;     ...
;             PG8_LDB(B0, 1, 0); PG8_LDB(B1, 1, 1); PG8_SCHED; PG8_LDA(At, 1, 0); PG8_STAGE(PG8_SA(0, 1), a2 + ah, v2[1]);
;             PG8_WAIT_V(8); PG8_WAIT_L(0); PG8_BAR; PG8_MMA(0, 0, At, B0); PG8_MMA(0, 1, At, B1); PG8_BAR; PG8_SCHED;
;             PG8_LDA(At, 1, 1); PG8_STAGE(PG8_SB(1, 0), b3, voffB); PG8_STAGE(PG8_SB(1, 1), b3 + bstep, voffB); PG8_STAGE(PG8_SA(1, 0), a3, v2[0]);
;             PG8_WAIT_V(8); PG8_WAIT_L(0); PG8_BAR; if (full) { PG8_MMA(1, 0, At, B0); PG8_MMA(1, 1, At, B1); } PG8_BAR; PG8_SCHED;
.LBB0_841:
	s_add_u32 s4, s4, 0x8000
	s_addc_u32 s5, s5, 0
	s_barrier
	s_add_i32 s35, 0, 0x18000
	s_add_i32 s36, 0, 0x1c000
	v_add_u32_e32 v2, s35, v247
	v_add_u32_e32 v6, s36, v247
	ds_read_b128 v[26:29], v2
	ds_read_b128 v[30:33], v2 offset:1024
	ds_read_b128 v[18:21], v2 offset:2048
	ds_read_b128 v[22:25], v2 offset:3072
	ds_read_b128 v[10:13], v6
	ds_read_b128 v[14:17], v6 offset:1024
	ds_read_b128 v[2:5], v6 offset:2048
	ds_read_b128 v[6:9], v6 offset:3072
	s_mov_b32 m0, s15
	v_lshl_add_u64 v[250:251], s[4:5], 0, v[200:201]
	s_waitcnt lgkmcnt(0)
	ds_read_b128 v[34:37], v223 offset:32768
	ds_read_b128 v[38:41], v223 offset:33792
	ds_read_b128 v[42:45], v223 offset:34816
	ds_read_b128 v[46:49], v223 offset:35840
	ds_read_b128 v[50:53], v223 offset:36864
	ds_read_b128 v[54:57], v223 offset:37888
	ds_read_b128 v[58:61], v223 offset:38912
	ds_read_b128 v[62:65], v223 offset:39936
	global_load_lds_dwordx4 v[250:251], off
	v_lshl_add_u64 v[250:251], s[4:5], 0, v[202:203]
	s_mov_b32 m0, s16
	s_nop 0
	global_load_lds_dwordx4 v[250:251], off
	s_waitcnt vmcnt(8)
	s_waitcnt lgkmcnt(0)
	s_barrier
	s_setprio 1
	s_waitcnt lgkmcnt(0)
	v_mfma_scale_f32_16x16x128_f8f6f4 v[172:175], v[26:33], v[34:41], v[172:175], v1, v246 op_sel_hi:[0,0,0]
	v_mfma_scale_f32_16x16x128_f8f6f4 v[176:179], v[18:25], v[34:41], v[176:179], v1, v246 op_sel_hi:[0,0,0]
	v_mfma_scale_f32_16x16x128_f8f6f4 v[168:171], v[26:33], v[42:49], v[168:171], v1, v246 op_sel_hi:[0,0,0]
	v_mfma_scale_f32_16x16x128_f8f6f4 v[164:167], v[18:25], v[42:49], v[164:167], v1, v246 op_sel_hi:[0,0,0]
	v_mfma_scale_f32_16x16x128_f8f6f4 v[144:147], v[26:33], v[50:57], v[144:147], v1, v246 op_sel_hi:[0,0,0]
	v_mfma_scale_f32_16x16x128_f8f6f4 v[136:139], v[18:25], v[50:57], v[136:139], v1, v246 op_sel_hi:[0,0,0]
	v_mfma_scale_f32_16x16x128_f8f6f4 v[116:119], v[26:33], v[58:65], v[116:119], v1, v246 op_sel_hi:[0,0,0]
	v_mfma_scale_f32_16x16x128_f8f6f4 v[112:115], v[18:25], v[58:65], v[112:115], v1, v246 op_sel_hi:[0,0,0]
	s_setprio 0
	s_setprio 1
	v_mfma_scale_f32_16x16x128_f8f6f4 v[188:191], v[10:17], v[34:41], v[188:191], v1, v246 op_sel_hi:[0,0,0]
	v_mfma_scale_f32_16x16x128_f8f6f4 v[192:195], v[2:9], v[34:41], v[192:195], v1, v246 op_sel_hi:[0,0,0]
	v_mfma_scale_f32_16x16x128_f8f6f4 v[184:187], v[10:17], v[42:49], v[184:187], v1, v246 op_sel_hi:[0,0,0]
	v_mfma_scale_f32_16x16x128_f8f6f4 v[180:183], v[2:9], v[42:49], v[180:183], v1, v246 op_sel_hi:[0,0,0]
	v_mfma_scale_f32_16x16x128_f8f6f4 v[152:155], v[10:17], v[50:57], v[152:155], v1, v246 op_sel_hi:[0,0,0]
	v_mfma_scale_f32_16x16x128_f8f6f4 v[148:151], v[2:9], v[50:57], v[148:151], v1, v246 op_sel_hi:[0,0,0]
	v_mfma_scale_f32_16x16x128_f8f6f4 v[120:123], v[10:17], v[58:65], v[120:123], v1, v246 op_sel_hi:[0,0,0]
	v_mfma_scale_f32_16x16x128_f8f6f4 v[80:83], v[2:9], v[58:65], v[80:83], v1, v246 op_sel_hi:[0,0,0]
	s_setprio 0
	s_barrier
	s_add_i32 s4, s35, s8
	v_lshl_add_u64 v[250:251], v[240:241], 0, s[48:49]
	s_mov_b32 m0, s4
	ds_read_b128 v[58:61], v223 offset:49152
	ds_read_b128 v[62:65], v223 offset:50176
	ds_read_b128 v[50:53], v223 offset:51200
	ds_read_b128 v[54:57], v223 offset:52224
	ds_read_b128 v[42:45], v223 offset:53248
	ds_read_b128 v[46:49], v223 offset:54272
	ds_read_b128 v[34:37], v223 offset:55296
	ds_read_b128 v[38:41], v223 offset:56320
	global_load_lds_dwordx4 v[250:251], off
	v_lshl_add_u64 v[250:251], v[238:239], 0, s[48:49]
	s_add_i32 m0, s4, 0x2000
	s_add_i32 s4, s36, s8
	global_load_lds_dwordx4 v[250:251], off
	v_lshl_add_u64 v[240:241], v[240:241], 0, s[50:51]
	s_mov_b32 m0, s4
	v_lshl_add_u64 v[238:239], v[238:239], 0, s[50:51]
	global_load_lds_dwordx4 v[240:241], off
	s_add_i32 m0, s4, 0x2000
	s_andn2_b64 vcc, exec, s[90:91]
	global_load_lds_dwordx4 v[238:239], off
	v_lshl_add_u64 v[238:239], v[242:243], 0, s[48:49]
	s_mov_b32 m0, s20
	s_nop 0
	global_load_lds_dwordx4 v[238:239], off
	v_lshl_add_u64 v[238:239], v[244:245], 0, s[48:49]
	s_mov_b32 m0, s21
	s_nop 0
	global_load_lds_dwordx4 v[238:239], off
	s_waitcnt vmcnt(8)
	s_waitcnt lgkmcnt(0)
	s_barrier
	s_cbranch_vccnz .Lg2c_nf0
; #define PG8_STAGE(bufoff, gbase, voff) do { _Pragma("unroll") for (int _i = 0; _i < 2; ++_i) \
;         __builtin_amdgcn_global_load_lds((const unsigned*)((const char*)(gbase) + (voff)[_i]), (LAS unsigned*)(lds + (bufoff) + ldsw + _i * 8192), 16, 0, 0); } while (0)
; #define PG8_LDA(dst, b, h) do { _Pragma("unroll") for (int m = 0; m < 4; ++m) _Pragma("unroll") for (int k = 0; k < 2; ++k) dst[m][k] = *(const LAS bf16x8*)(lds + PG8_SA(b, h) + aoff + m * 2048 + k * 1024); } while (0)
; #define PG8_LDB(dst, b, h) do { _Pragma("unroll") for (int n = 0; n < 2; ++n) _Pragma("unroll") for (int k = 0; k < 2; ++k) dst[n][k] = *(const LAS bf16x8*)(lds + PG8_SB(b, h) + boff + n * 2048 + k * 1024); } while (0)
; #define PG8_WAIT_V(n) asm volatile("s_waitcnt vmcnt(" #n ")" ::: "memory")
; #define PG8_WAIT_L(n) asm volatile("s_waitcnt lgkmcnt(" #n ")" ::: "memory")
; #define PG8_BAR __builtin_amdgcn_s_barrier()
; #define PG8_SCHED __builtin_amdgcn_sched_barrier(0)
;     ...
;             PG8_WAIT_V(8); PG8_WAIT_L(0); PG8_BAR; if (full) { PG8_MMA(1, 0, At, B0); PG8_MMA(1, 1, At, B1); } PG8_BAR; PG8_SCHED;
;             PG8_LDB(B0, 1, 0); PG8_LDB(B1, 1, 1); PG8_SCHED; PG8_LDA(At, 1, 0); PG8_STAGE(PG8_SA(0, 1), a2 + ah, v2[1]);
;             PG8_WAIT_V(8); PG8_WAIT_L(0); PG8_BAR; PG8_MMA(0, 0, At, B0); PG8_MMA(0, 1, At, B1); PG8_BAR; PG8_SCHED;
;             PG8_LDA(At, 1, 1); PG8_STAGE(PG8_SB(1, 0), b3, voffB); PG8_STAGE(PG8_SB(1, 1), b3 + bstep, voffB); PG8_STAGE(PG8_SA(1, 0), a3, v2[0]);
;             PG8_WAIT_V(8); PG8_WAIT_L(0); PG8_BAR; if (full) { PG8_MMA(1, 0, At, B0); PG8_MMA(1, 1, At, B1); } PG8_BAR; PG8_SCHED;
;     __device__ __forceinline__ u32x4 pack(const f32x4 (&acc)[2][2][4][2], int ai, int m) const {
;     ...
;             f32x4 v0 = acc[ai][bj][m][0], v1 = acc[ai][bj][m][1];
; #pragma unroll
;             for (int j = 0; j < 4; ++j) { v0[j] = fminf(fmaxf(v0[j], -448.f), 448.f); v1[j] = fminf(fmaxf(v1[j], -448.f), 448.f); }
	s_setprio 1
	s_waitcnt lgkmcnt(0)
	v_mfma_scale_f32_16x16x128_f8f6f4 v[128:131], v[26:33], v[58:65], v[128:131], v1, v246 op_sel_hi:[0,0,0]
	v_med3_f32 v172, v172, s29, v227
	v_med3_f32 v176, v176, s29, v227
	v_med3_f32 v173, v173, s29, v227
	v_med3_f32 v177, v177, s29, v227
	v_mfma_scale_f32_16x16x128_f8f6f4 v[124:127], v[18:25], v[58:65], v[124:127], v1, v246 op_sel_hi:[0,0,0]
	v_med3_f32 v174, v174, s29, v227
	v_med3_f32 v178, v178, s29, v227
	v_med3_f32 v175, v175, s29, v227
	v_med3_f32 v179, v179, s29, v227
	v_mfma_scale_f32_16x16x128_f8f6f4 v[108:111], v[26:33], v[50:57], v[108:111], v1, v246 op_sel_hi:[0,0,0]
	v_med3_f32 v188, v188, s29, v227
	v_med3_f32 v192, v192, s29, v227
	v_med3_f32 v189, v189, s29, v227
	v_med3_f32 v193, v193, s29, v227
	v_mfma_scale_f32_16x16x128_f8f6f4 v[104:107], v[18:25], v[50:57], v[104:107], v1, v246 op_sel_hi:[0,0,0]
	v_med3_f32 v190, v190, s29, v227
	v_med3_f32 v194, v194, s29, v227
	v_med3_f32 v191, v191, s29, v227
	v_med3_f32 v195, v195, s29, v227
	v_mfma_scale_f32_16x16x128_f8f6f4 v[92:95], v[26:33], v[42:49], v[92:95], v1, v246 op_sel_hi:[0,0,0]
	v_med3_f32 v168, v168, s29, v227
	v_med3_f32 v164, v164, s29, v227
	v_med3_f32 v169, v169, s29, v227
	v_med3_f32 v165, v165, s29, v227
	v_mfma_scale_f32_16x16x128_f8f6f4 v[84:87], v[18:25], v[42:49], v[84:87], v1, v246 op_sel_hi:[0,0,0]
	v_med3_f32 v170, v170, s29, v227
	v_med3_f32 v166, v166, s29, v227
	v_med3_f32 v171, v171, s29, v227
	v_med3_f32 v167, v167, s29, v227
	v_mfma_scale_f32_16x16x128_f8f6f4 v[76:79], v[26:33], v[34:41], v[76:79], v1, v246 op_sel_hi:[0,0,0]
	v_med3_f32 v184, v184, s29, v227
	v_med3_f32 v180, v180, s29, v227
	v_med3_f32 v185, v185, s29, v227
	v_med3_f32 v181, v181, s29, v227
	v_mfma_scale_f32_16x16x128_f8f6f4 v[72:75], v[18:25], v[34:41], v[72:75], v1, v246 op_sel_hi:[0,0,0]
	v_med3_f32 v186, v186, s29, v227
	v_med3_f32 v182, v182, s29, v227
	v_med3_f32 v187, v187, s29, v227
	v_med3_f32 v183, v183, s29, v227
	s_setprio 0
	s_setprio 1
	v_mfma_scale_f32_16x16x128_f8f6f4 v[160:163], v[10:17], v[58:65], v[160:163], v1, v246 op_sel_hi:[0,0,0]
	v_med3_f32 v136, v136, s29, v227
	v_med3_f32 v137, v137, s29, v227
	v_med3_f32 v144, v144, s29, v227
	v_med3_f32 v145, v145, s29, v227
	v_mfma_scale_f32_16x16x128_f8f6f4 v[156:159], v[2:9], v[58:65], v[156:159], v1, v246 op_sel_hi:[0,0,0]
	v_med3_f32 v138, v138, s29, v227
	v_med3_f32 v139, v139, s29, v227
	v_med3_f32 v148, v148, s29, v227
	v_med3_f32 v149, v149, s29, v227
	v_mfma_scale_f32_16x16x128_f8f6f4 v[140:143], v[10:17], v[50:57], v[140:143], v1, v246 op_sel_hi:[0,0,0]
	v_med3_f32 v152, v152, s29, v227
	v_med3_f32 v153, v153, s29, v227
	v_med3_f32 v150, v150, s29, v227
	v_med3_f32 v151, v151, s29, v227
	v_mfma_scale_f32_16x16x128_f8f6f4 v[132:135], v[2:9], v[50:57], v[132:135], v1, v246 op_sel_hi:[0,0,0]
	v_med3_f32 v112, v112, s29, v227
	v_med3_f32 v113, v113, s29, v227
	v_med3_f32 v116, v116, s29, v227
	v_med3_f32 v117, v117, s29, v227
	v_mfma_scale_f32_16x16x128_f8f6f4 v[100:103], v[10:17], v[42:49], v[100:103], v1, v246 op_sel_hi:[0,0,0]
	v_med3_f32 v146, v146, s29, v227
	v_med3_f32 v147, v147, s29, v227
	v_med3_f32 v114, v114, s29, v227
	v_med3_f32 v115, v115, s29, v227
	v_mfma_scale_f32_16x16x128_f8f6f4 v[96:99], v[2:9], v[42:49], v[96:99], v1, v246 op_sel_hi:[0,0,0]
	v_med3_f32 v154, v154, s29, v227
	v_med3_f32 v155, v155, s29, v227
	v_med3_f32 v120, v120, s29, v227
	v_med3_f32 v80, v80, s29, v227
	v_mfma_scale_f32_16x16x128_f8f6f4 v[88:91], v[10:17], v[34:41], v[88:91], v1, v246 op_sel_hi:[0,0,0]
	v_med3_f32 v121, v121, s29, v227
	v_med3_f32 v81, v81, s29, v227
	v_med3_f32 v118, v118, s29, v227
	v_med3_f32 v119, v119, s29, v227
	v_mfma_scale_f32_16x16x128_f8f6f4 v[68:71], v[2:9], v[34:41], v[68:71], v1, v246 op_sel_hi:[0,0,0]
	v_med3_f32 v122, v122, s29, v227
	v_med3_f32 v82, v82, s29, v227
	v_med3_f32 v123, v123, s29, v227
	v_med3_f32 v83, v83, s29, v227
	s_setprio 0
	s_branch .LBB0_843
.Lg2c_nf0:
	v_med3_f32 v172, v172, s29, v227
	v_med3_f32 v176, v176, s29, v227
	v_med3_f32 v173, v173, s29, v227
	v_med3_f32 v177, v177, s29, v227
	v_med3_f32 v174, v174, s29, v227
	v_med3_f32 v178, v178, s29, v227
	v_med3_f32 v175, v175, s29, v227
	v_med3_f32 v179, v179, s29, v227
	v_med3_f32 v188, v188, s29, v227
	v_med3_f32 v192, v192, s29, v227
	v_med3_f32 v189, v189, s29, v227
	v_med3_f32 v193, v193, s29, v227
	v_med3_f32 v190, v190, s29, v227
	v_med3_f32 v194, v194, s29, v227
	v_med3_f32 v191, v191, s29, v227
	v_med3_f32 v195, v195, s29, v227
	v_med3_f32 v168, v168, s29, v227
	v_med3_f32 v164, v164, s29, v227
	v_med3_f32 v169, v169, s29, v227
	v_med3_f32 v165, v165, s29, v227
	v_med3_f32 v170, v170, s29, v227
	v_med3_f32 v166, v166, s29, v227
	v_med3_f32 v171, v171, s29, v227
	v_med3_f32 v167, v167, s29, v227
	v_med3_f32 v184, v184, s29, v227
	v_med3_f32 v180, v180, s29, v227
	v_med3_f32 v185, v185, s29, v227
	v_med3_f32 v181, v181, s29, v227
	v_med3_f32 v186, v186, s29, v227
	v_med3_f32 v182, v182, s29, v227
	v_med3_f32 v187, v187, s29, v227
	v_med3_f32 v183, v183, s29, v227
	v_med3_f32 v136, v136, s29, v227
	v_med3_f32 v137, v137, s29, v227
	v_med3_f32 v144, v144, s29, v227
	v_med3_f32 v145, v145, s29, v227
	v_med3_f32 v138, v138, s29, v227
	v_med3_f32 v139, v139, s29, v227
	v_med3_f32 v148, v148, s29, v227
	v_med3_f32 v149, v149, s29, v227
	v_med3_f32 v152, v152, s29, v227
	v_med3_f32 v153, v153, s29, v227
	v_med3_f32 v150, v150, s29, v227
	v_med3_f32 v151, v151, s29, v227
	v_med3_f32 v112, v112, s29, v227
	v_med3_f32 v113, v113, s29, v227
	v_med3_f32 v116, v116, s29, v227
	v_med3_f32 v117, v117, s29, v227
	v_med3_f32 v146, v146, s29, v227
	v_med3_f32 v147, v147, s29, v227
	v_med3_f32 v114, v114, s29, v227
	v_med3_f32 v115, v115, s29, v227
	v_med3_f32 v154, v154, s29, v227
	v_med3_f32 v155, v155, s29, v227
	v_med3_f32 v120, v120, s29, v227
	v_med3_f32 v80, v80, s29, v227
	v_med3_f32 v121, v121, s29, v227
	v_med3_f32 v81, v81, s29, v227
	v_med3_f32 v118, v118, s29, v227
	v_med3_f32 v119, v119, s29, v227
	v_med3_f32 v122, v122, s29, v227
	v_med3_f32 v82, v82, s29, v227
	v_med3_f32 v123, v123, s29, v227
	v_med3_f32 v83, v83, s29, v227

;     __device__ __forceinline__ u32x4 pack(const f32x4 (&acc)[2][2][4][2], int ai, int m) const {
;         u32x4 w;
; #pragma unroll
;         for (int bj = 0; bj < 2; ++bj) {
;             f32x4 v0 = acc[ai][bj][m][0], v1 = acc[ai][bj][m][1];
; #pragma unroll
;             for (int j = 0; j < 4; ++j) { v0[j] = fminf(fmaxf(v0[j], -448.f), 448.f); v1[j] = fminf(fmaxf(v1[j], -448.f), 448.f); }
;             int w0 = __builtin_amdgcn_cvt_pk_fp8_f32(v0[0], v0[1], 0, false); w0 = __builtin_amdgcn_cvt_pk_fp8_f32(v0[2], v0[3], w0, true);
;             int w1 = __builtin_amdgcn_cvt_pk_fp8_f32(v1[0], v1[1], 0, false); w1 = __builtin_amdgcn_cvt_pk_fp8_f32(v1[2], v1[3], w1, true);
;             if (bj == 0) { w.x = (unsigned)w0; w.y = (unsigned)w1; } else { w.z = (unsigned)w0; w.w = (unsigned)w1; } }
;         return w;
;     }
;     __device__ __forceinline__ void operator()(const f32x4 (&acc)[2][2][4][2], const Unit& u, int wr, int wc, int fr, int fq) const {
;         const int lane = fq * 16 + fr, wv = wr * 4 + wc;
;         constexpr int B0 = 3 * pg8::HTB, B1 = UT_TOK;
;         const int wofs = (32 * wr + fr) * 256 + (((4 * wc + fq) ^ fr) << 4);
;         const int rr0 = 8 * wv + (lane >> 4);
;         const int rofs = rr0 * 256 + (((lane & 15) ^ (rr0 & 15)) << 4), rofs4 = (rr0 + 4) * 256 + (((lane & 15) ^ ((rr0 + 4) & 15)) << 4);
;         const int t0 = 64 * (rr0 >> 5) + 16 * ((rr0 >> 4) & 1) + (rr0 & 15);
;         unsigned char* yp = Y + (size_t)u.row0 * D + u.nt * 256 + 16 * (lane & 15);
;         { const u32x4 wa = pack(acc, 0, 0), wb = pack(acc, 0, 1); *(LAS u32x4*)(lds + B0 + wofs) = wa; *(LAS u32x4*)(lds + B0 + wofs + 16 * 256) = wb; }
; #pragma unroll
;         for (int sl = 0; sl < 4; ++sl) { const int ai = sl >> 1, mh = sl & 1;
;             asm volatile("s_waitcnt lgkmcnt(0)" ::: "memory"); __builtin_amdgcn_s_barrier();
;             const int rb = (sl & 1) ? B1 : B0, wb_ = (sl & 1) ? B0 : B1;
;             const u32x4 v0 = *(const LAS u32x4*)(lds + rb + rofs), v1 = *(const LAS u32x4*)(lds + rb + rofs4);
;             if (sl < 3) { const int a2 = (sl + 1) >> 1, m2 = ((sl + 1) & 1) * 2;
;                 const u32x4 wa = pack(acc, a2, m2), wb = pack(acc, a2, m2 + 1); *(LAS u32x4*)(lds + wb_ + wofs) = wa; *(LAS u32x4*)(lds + wb_ + wofs + 16 * 256) = wb; }
;             const int rl = ai * 128 + mh * 32 + t0;
.LBB0_845:
	v_cvt_pk_fp8_f32 v2, v172, v173
	v_cvt_pk_fp8_f32 v3, v176, v177
	v_cvt_pk_fp8_f32 v2, v174, v175 op_sel:[0,0,1]
	v_cvt_pk_fp8_f32 v3, v178, v179 op_sel:[0,0,1]
	v_cvt_pk_fp8_f32 v4, v188, v189
	v_cvt_pk_fp8_f32 v5, v192, v193
	v_cvt_pk_fp8_f32 v4, v190, v191 op_sel:[0,0,1]
	v_cvt_pk_fp8_f32 v5, v194, v195 op_sel:[0,0,1]
	v_cvt_pk_fp8_f32 v6, v168, v169
	v_cvt_pk_fp8_f32 v7, v164, v165
	v_cvt_pk_fp8_f32 v6, v170, v171 op_sel:[0,0,1]
	v_cvt_pk_fp8_f32 v7, v166, v167 op_sel:[0,0,1]
	v_cvt_pk_fp8_f32 v8, v184, v185
	v_cvt_pk_fp8_f32 v9, v180, v181
	v_cvt_pk_fp8_f32 v8, v186, v187 op_sel:[0,0,1]
	v_cvt_pk_fp8_f32 v9, v182, v183 op_sel:[0,0,1]
	s_nop 15
	s_nop 15
	ds_write_b128 v207, v[2:5] offset:49152
	ds_write_b128 v207, v[6:9] offset:53248
	v_cvt_pk_fp8_f32 v15, v136, v137
	v_mov_b32_e32 v14, 0
	v_cvt_pk_fp8_f32 v14, v144, v145
	v_cvt_pk_fp8_f32 v15, v138, v139 op_sel:[0,0,1]
	v_cvt_pk_fp8_f32 v17, v148, v149
	v_mov_b32_e32 v16, 0
	v_cvt_pk_fp8_f32 v16, v152, v153
	v_cvt_pk_fp8_f32 v17, v150, v151 op_sel:[0,0,1]
	v_cvt_pk_fp8_f32 v19, v112, v113
	v_cvt_pk_fp8_f32 v18, v116, v117
	v_cvt_pk_fp8_f32 v14, v146, v147 op_sel:[0,0,1]
	v_cvt_pk_fp8_f32 v19, v114, v115 op_sel:[0,0,1]
	v_cvt_pk_fp8_f32 v16, v154, v155 op_sel:[0,0,1]
	v_cvt_pk_fp8_f32 v20, v120, v121
	v_cvt_pk_fp8_f32 v21, v80, v81
	s_ashr_i32 s89, s88, 31
	s_lshl_b64 s[4:5], s[88:89], 10
	v_cvt_pk_fp8_f32 v18, v118, v119 op_sel:[0,0,1]
	s_add_u32 s4, s18, s4
	s_addc_u32 s5, s19, s5
	s_lshl_b32 s34, s34, 8
	s_waitcnt lgkmcnt(0)
	s_barrier
	v_cvt_pk_fp8_f32 v20, v122, v123 op_sel:[0,0,1]
	v_cvt_pk_fp8_f32 v21, v82, v83 op_sel:[0,0,1]
	ds_read_b128 v[6:9], v231 offset:49152
	ds_read_b128 v[2:5], v235 offset:49152
	s_ashr_i32 s35, s34, 31
	s_add_u32 s4, s4, s34
	s_addc_u32 s5, s5, s35
	v_lshl_add_u64 v[10:11], s[4:5], 0, v[204:205]
	v_add_u32_e32 v12, 0x20410, v207
	v_cmp_gt_i32_e32 vcc, s7, v206
	ds_write_b128 v12, v[14:17]
	ds_write_b128 v211, v[18:21]
	s_and_saveexec_b64 s[4:5], vcc
	s_cbranch_execz .LBB0_847
	v_lshl_add_u64 v[14:15], v[10:11], 0, v[208:209]
	s_waitcnt lgkmcnt(0)
	global_store_dwordx4 v[14:15], v[6:9], off nt

; #define PG8_STAGE(bufoff, gbase, voff) do { _Pragma("unroll") for (int _i = 0; _i < 2; ++_i) \
;         __builtin_amdgcn_global_load_lds((const unsigned*)((const char*)(gbase) + (voff)[_i]), (LAS unsigned*)(lds + (bufoff) + ldsw + _i * 8192), 16, 0, 0); } while (0)
; #define PG8_LDA(dst, b, h) do { _Pragma("unroll") for (int m = 0; m < 4; ++m) _Pragma("unroll") for (int k = 0; k < 2; ++k) dst[m][k] = *(const LAS bf16x8*)(lds + PG8_SA(b, h) + aoff + m * 2048 + k * 1024); } while (0)
; #define PG8_LDB(dst, b, h) do { _Pragma("unroll") for (int n = 0; n < 2; ++n) _Pragma("unroll") for (int k = 0; k < 2; ++k) dst[n][k] = *(const LAS bf16x8*)(lds + PG8_SB(b, h) + boff + n * 2048 + k * 1024); } while (0)
; #define PG8_WAIT_V(n) asm volatile("s_waitcnt vmcnt(" #n ")" ::: "memory")
; #define PG8_WAIT_L(n) asm volatile("s_waitcnt lgkmcnt(" #n ")" ::: "memory")
; #define PG8_BAR __builtin_amdgcn_s_barrier()
; #define PG8_SCHED __builtin_amdgcn_sched_barrier(0)
;     ...
;             PG8_LDB(B0, 1, 0); PG8_LDB(B1, 1, 1); PG8_SCHED; PG8_LDA(At, 1, 0); PG8_STAGE(PG8_SA(0, 1), a2 + ah, v2[1]);
;             PG8_WAIT_V(8); PG8_WAIT_L(0); PG8_BAR; PG8_MMA(0, 0, At, B0); PG8_MMA(0, 1, At, B1); PG8_BAR; PG8_SCHED;
;             PG8_LDA(At, 1, 1); PG8_STAGE(PG8_SB(1, 0), b3, voffB); PG8_STAGE(PG8_SB(1, 1), b3 + bstep, voffB); PG8_STAGE(PG8_SA(1, 0), a3, v2[0]);
;             PG8_WAIT_V(8); PG8_WAIT_L(0); PG8_BAR; if (full) { PG8_MMA(1, 0, At, B0); PG8_MMA(1, 1, At, B1); } PG8_BAR; PG8_SCHED;
.LBB0_1068:
	s_add_u32 s4, s4, 0x8000
	s_addc_u32 s5, s5, 0
	s_barrier
	s_add_i32 s18, 0, 0x18000
	s_add_i32 s19, 0, 0x1c000
	v_add_u32_e32 v2, s18, v247
	v_add_u32_e32 v6, s19, v247
	ds_read_b128 v[26:29], v2
	ds_read_b128 v[30:33], v2 offset:1024
	ds_read_b128 v[18:21], v2 offset:2048
	ds_read_b128 v[22:25], v2 offset:3072
	ds_read_b128 v[10:13], v6
	ds_read_b128 v[14:17], v6 offset:1024
	ds_read_b128 v[2:5], v6 offset:2048
	ds_read_b128 v[6:9], v6 offset:3072
	s_mov_b32 m0, s14
	v_lshl_add_u64 v[250:251], s[4:5], 0, v[200:201]
	s_waitcnt lgkmcnt(0)
	ds_read_b128 v[34:37], v223 offset:32768
	ds_read_b128 v[38:41], v223 offset:33792
	ds_read_b128 v[42:45], v223 offset:34816
	ds_read_b128 v[46:49], v223 offset:35840
	ds_read_b128 v[50:53], v223 offset:36864
	ds_read_b128 v[54:57], v223 offset:37888
	ds_read_b128 v[58:61], v223 offset:38912
	ds_read_b128 v[62:65], v223 offset:39936
	global_load_lds_dwordx4 v[250:251], off
	v_lshl_add_u64 v[250:251], s[4:5], 0, v[202:203]
	s_mov_b32 m0, s15
	s_nop 0
	global_load_lds_dwordx4 v[250:251], off
	s_waitcnt vmcnt(8)
	s_waitcnt lgkmcnt(0)
	s_barrier
	s_setprio 1
	s_waitcnt lgkmcnt(0)
	v_mfma_scale_f32_16x16x128_f8f6f4 v[172:175], v[26:33], v[34:41], v[172:175], v1, v246 op_sel_hi:[0,0,0]
	v_mfma_scale_f32_16x16x128_f8f6f4 v[176:179], v[18:25], v[34:41], v[176:179], v1, v246 op_sel_hi:[0,0,0]
	v_mfma_scale_f32_16x16x128_f8f6f4 v[168:171], v[26:33], v[42:49], v[168:171], v1, v246 op_sel_hi:[0,0,0]
	v_mfma_scale_f32_16x16x128_f8f6f4 v[164:167], v[18:25], v[42:49], v[164:167], v1, v246 op_sel_hi:[0,0,0]
	v_mfma_scale_f32_16x16x128_f8f6f4 v[144:147], v[26:33], v[50:57], v[144:147], v1, v246 op_sel_hi:[0,0,0]
	v_mfma_scale_f32_16x16x128_f8f6f4 v[136:139], v[18:25], v[50:57], v[136:139], v1, v246 op_sel_hi:[0,0,0]
	v_mfma_scale_f32_16x16x128_f8f6f4 v[116:119], v[26:33], v[58:65], v[116:119], v1, v246 op_sel_hi:[0,0,0]
	v_mfma_scale_f32_16x16x128_f8f6f4 v[112:115], v[18:25], v[58:65], v[112:115], v1, v246 op_sel_hi:[0,0,0]
	s_setprio 0
	s_setprio 1
	v_mfma_scale_f32_16x16x128_f8f6f4 v[188:191], v[10:17], v[34:41], v[188:191], v1, v246 op_sel_hi:[0,0,0]
	v_mfma_scale_f32_16x16x128_f8f6f4 v[192:195], v[2:9], v[34:41], v[192:195], v1, v246 op_sel_hi:[0,0,0]
	v_mfma_scale_f32_16x16x128_f8f6f4 v[184:187], v[10:17], v[42:49], v[184:187], v1, v246 op_sel_hi:[0,0,0]
	v_mfma_scale_f32_16x16x128_f8f6f4 v[180:183], v[2:9], v[42:49], v[180:183], v1, v246 op_sel_hi:[0,0,0]
	v_mfma_scale_f32_16x16x128_f8f6f4 v[152:155], v[10:17], v[50:57], v[152:155], v1, v246 op_sel_hi:[0,0,0]
	v_mfma_scale_f32_16x16x128_f8f6f4 v[148:151], v[2:9], v[50:57], v[148:151], v1, v246 op_sel_hi:[0,0,0]
	v_mfma_scale_f32_16x16x128_f8f6f4 v[120:123], v[10:17], v[58:65], v[120:123], v1, v246 op_sel_hi:[0,0,0]
	v_mfma_scale_f32_16x16x128_f8f6f4 v[80:83], v[2:9], v[58:65], v[80:83], v1, v246 op_sel_hi:[0,0,0]
	s_setprio 0
	s_barrier
	s_add_i32 s4, s18, s7
	v_lshl_add_u64 v[250:251], v[240:241], 0, s[48:49]
	s_mov_b32 m0, s4
	ds_read_b128 v[58:61], v223 offset:49152
	ds_read_b128 v[62:65], v223 offset:50176
	ds_read_b128 v[50:53], v223 offset:51200
	ds_read_b128 v[54:57], v223 offset:52224
	ds_read_b128 v[42:45], v223 offset:53248
	ds_read_b128 v[46:49], v223 offset:54272
	ds_read_b128 v[34:37], v223 offset:55296
	ds_read_b128 v[38:41], v223 offset:56320
	global_load_lds_dwordx4 v[250:251], off
	v_lshl_add_u64 v[250:251], v[238:239], 0, s[48:49]
	s_add_i32 m0, s4, 0x2000
	s_add_i32 s4, s19, s7
	global_load_lds_dwordx4 v[250:251], off
	v_lshl_add_u64 v[240:241], v[240:241], 0, s[50:51]
	s_mov_b32 m0, s4
	v_lshl_add_u64 v[238:239], v[238:239], 0, s[50:51]
	global_load_lds_dwordx4 v[240:241], off
	s_add_i32 m0, s4, 0x2000
	s_andn2_b64 vcc, exec, s[88:89]
	global_load_lds_dwordx4 v[238:239], off
	v_lshl_add_u64 v[238:239], v[242:243], 0, s[48:49]
	s_mov_b32 m0, s21
	s_nop 0
	global_load_lds_dwordx4 v[238:239], off
	v_lshl_add_u64 v[238:239], v[244:245], 0, s[48:49]
	s_mov_b32 m0, s22
	s_nop 0
	global_load_lds_dwordx4 v[238:239], off
	s_waitcnt vmcnt(8)
	s_waitcnt lgkmcnt(0)
	s_barrier
	s_cbranch_vccnz .Lg2c_nf1
; #define PG8_STAGE(bufoff, gbase, voff) do { _Pragma("unroll") for (int _i = 0; _i < 2; ++_i) \
;         __builtin_amdgcn_global_load_lds((const unsigned*)((const char*)(gbase) + (voff)[_i]), (LAS unsigned*)(lds + (bufoff) + ldsw + _i * 8192), 16, 0, 0); } while (0)
; #define PG8_LDA(dst, b, h) do { _Pragma("unroll") for (int m = 0; m < 4; ++m) _Pragma("unroll") for (int k = 0; k < 2; ++k) dst[m][k] = *(const LAS bf16x8*)(lds + PG8_SA(b, h) + aoff + m * 2048 + k * 1024); } while (0)
; #define PG8_LDB(dst, b, h) do { _Pragma("unroll") for (int n = 0; n < 2; ++n) _Pragma("unroll") for (int k = 0; k < 2; ++k) dst[n][k] = *(const LAS bf16x8*)(lds + PG8_SB(b, h) + boff + n * 2048 + k * 1024); } while (0)
; #define PG8_WAIT_V(n) asm volatile("s_waitcnt vmcnt(" #n ")" ::: "memory")
; #define PG8_WAIT_L(n) asm volatile("s_waitcnt lgkmcnt(" #n ")" ::: "memory")
; #define PG8_BAR __builtin_amdgcn_s_barrier()
;     ...
;             PG8_WAIT_V(8); PG8_WAIT_L(0); PG8_BAR; if (full) { PG8_MMA(1, 0, At, B0); PG8_MMA(1, 1, At, B1); } PG8_BAR; PG8_SCHED;
;             PG8_LDB(B0, 1, 0); PG8_LDB(B1, 1, 1); PG8_SCHED; PG8_LDA(At, 1, 0); PG8_STAGE(PG8_SA(0, 1), a2 + ah, v2[1]);
;             PG8_WAIT_V(8); PG8_WAIT_L(0); PG8_BAR; PG8_MMA(0, 0, At, B0); PG8_MMA(0, 1, At, B1); PG8_BAR; PG8_SCHED;
;             PG8_LDA(At, 1, 1); PG8_STAGE(PG8_SB(1, 0), b3, voffB); PG8_STAGE(PG8_SB(1, 1), b3 + bstep, voffB); PG8_STAGE(PG8_SA(1, 0), a3, v2[0]);
;             PG8_WAIT_V(8); PG8_WAIT_L(0); PG8_BAR; if (full) { PG8_MMA(1, 0, At, B0); PG8_MMA(1, 1, At, B1); } PG8_BAR; PG8_SCHED;
;     __device__ __forceinline__ u32x4 pack(const f32x4 (&acc)[2][2][4][2], int ai, int m) const {
;         u32x4 w;
; #pragma unroll
;         for (int bj = 0; bj < 2; ++bj) {
;             f32x4 v0 = acc[ai][bj][m][0], v1 = acc[ai][bj][m][1];
; #pragma unroll
;             for (int j = 0; j < 4; ++j) { v0[j] = fminf(fmaxf(v0[j], -448.f), 448.f); v1[j] = fminf(fmaxf(v1[j], -448.f), 448.f); }
;             int w0 = __builtin_amdgcn_cvt_pk_fp8_f32(v0[0], v0[1], 0, false); w0 = __builtin_amdgcn_cvt_pk_fp8_f32(v0[2], v0[3], w0, true);
;             int w1 = __builtin_amdgcn_cvt_pk_fp8_f32(v1[0], v1[1], 0, false); w1 = __builtin_amdgcn_cvt_pk_fp8_f32(v1[2], v1[3], w1, true);
;             if (bj == 0) { w.x = (unsigned)w0; w.y = (unsigned)w1; } else { w.z = (unsigned)w0; w.w = (unsigned)w1; } }
	s_setprio 1
	s_waitcnt lgkmcnt(0)
	v_mfma_scale_f32_16x16x128_f8f6f4 v[128:131], v[26:33], v[58:65], v[128:131], v1, v246 op_sel_hi:[0,0,0]
	v_med3_f32 v172, v172, s30, v227
	v_med3_f32 v176, v176, s30, v227
	v_med3_f32 v173, v173, s30, v227
	v_med3_f32 v177, v177, s30, v227
	v_mfma_scale_f32_16x16x128_f8f6f4 v[124:127], v[18:25], v[58:65], v[124:127], v1, v246 op_sel_hi:[0,0,0]
	v_med3_f32 v174, v174, s30, v227
	v_med3_f32 v178, v178, s30, v227
	v_med3_f32 v175, v175, s30, v227
	v_med3_f32 v179, v179, s30, v227
	v_mfma_scale_f32_16x16x128_f8f6f4 v[108:111], v[26:33], v[50:57], v[108:111], v1, v246 op_sel_hi:[0,0,0]
	v_med3_f32 v188, v188, s30, v227
	v_med3_f32 v192, v192, s30, v227
	v_med3_f32 v189, v189, s30, v227
	v_med3_f32 v193, v193, s30, v227
	v_mfma_scale_f32_16x16x128_f8f6f4 v[104:107], v[18:25], v[50:57], v[104:107], v1, v246 op_sel_hi:[0,0,0]
	v_med3_f32 v190, v190, s30, v227
	v_med3_f32 v194, v194, s30, v227
	v_med3_f32 v191, v191, s30, v227
	v_med3_f32 v195, v195, s30, v227
	v_mfma_scale_f32_16x16x128_f8f6f4 v[92:95], v[26:33], v[42:49], v[92:95], v1, v246 op_sel_hi:[0,0,0]
	v_med3_f32 v168, v168, s30, v227
	v_med3_f32 v164, v164, s30, v227
	v_med3_f32 v169, v169, s30, v227
	v_med3_f32 v165, v165, s30, v227
	v_mfma_scale_f32_16x16x128_f8f6f4 v[84:87], v[18:25], v[42:49], v[84:87], v1, v246 op_sel_hi:[0,0,0]
	v_med3_f32 v170, v170, s30, v227
	v_med3_f32 v166, v166, s30, v227
	v_med3_f32 v171, v171, s30, v227
	v_med3_f32 v167, v167, s30, v227
	v_mfma_scale_f32_16x16x128_f8f6f4 v[76:79], v[26:33], v[34:41], v[76:79], v1, v246 op_sel_hi:[0,0,0]
	v_med3_f32 v184, v184, s30, v227
	v_med3_f32 v180, v180, s30, v227
	v_med3_f32 v185, v185, s30, v227
	v_med3_f32 v181, v181, s30, v227
	v_mfma_scale_f32_16x16x128_f8f6f4 v[72:75], v[18:25], v[34:41], v[72:75], v1, v246 op_sel_hi:[0,0,0]
	v_med3_f32 v186, v186, s30, v227
	v_med3_f32 v182, v182, s30, v227
	v_med3_f32 v187, v187, s30, v227
	v_med3_f32 v183, v183, s30, v227
	s_setprio 0
	s_setprio 1
	v_mfma_scale_f32_16x16x128_f8f6f4 v[160:163], v[10:17], v[58:65], v[160:163], v1, v246 op_sel_hi:[0,0,0]
	v_med3_f32 v136, v136, s30, v227
	v_med3_f32 v137, v137, s30, v227
	v_med3_f32 v144, v144, s30, v227
	v_med3_f32 v145, v145, s30, v227
	v_mfma_scale_f32_16x16x128_f8f6f4 v[156:159], v[2:9], v[58:65], v[156:159], v1, v246 op_sel_hi:[0,0,0]
	v_med3_f32 v138, v138, s30, v227
	v_med3_f32 v139, v139, s30, v227
	v_med3_f32 v148, v148, s30, v227
	v_med3_f32 v149, v149, s30, v227
	v_mfma_scale_f32_16x16x128_f8f6f4 v[140:143], v[10:17], v[50:57], v[140:143], v1, v246 op_sel_hi:[0,0,0]
	v_med3_f32 v152, v152, s30, v227
	v_med3_f32 v153, v153, s30, v227
	v_med3_f32 v150, v150, s30, v227
	v_med3_f32 v151, v151, s30, v227
	v_mfma_scale_f32_16x16x128_f8f6f4 v[132:135], v[2:9], v[50:57], v[132:135], v1, v246 op_sel_hi:[0,0,0]
	v_med3_f32 v112, v112, s30, v227
	v_med3_f32 v113, v113, s30, v227
	v_med3_f32 v116, v116, s30, v227
	v_med3_f32 v117, v117, s30, v227
	v_mfma_scale_f32_16x16x128_f8f6f4 v[100:103], v[10:17], v[42:49], v[100:103], v1, v246 op_sel_hi:[0,0,0]
	v_med3_f32 v146, v146, s30, v227
	v_med3_f32 v147, v147, s30, v227
	v_med3_f32 v114, v114, s30, v227
	v_med3_f32 v115, v115, s30, v227
	v_mfma_scale_f32_16x16x128_f8f6f4 v[96:99], v[2:9], v[42:49], v[96:99], v1, v246 op_sel_hi:[0,0,0]
	v_med3_f32 v154, v154, s30, v227
	v_med3_f32 v155, v155, s30, v227
	v_med3_f32 v120, v120, s30, v227
	v_med3_f32 v80, v80, s30, v227
	v_mfma_scale_f32_16x16x128_f8f6f4 v[88:91], v[10:17], v[34:41], v[88:91], v1, v246 op_sel_hi:[0,0,0]
	v_med3_f32 v121, v121, s30, v227
	v_med3_f32 v81, v81, s30, v227
	v_med3_f32 v118, v118, s30, v227
	v_med3_f32 v119, v119, s30, v227
	v_mfma_scale_f32_16x16x128_f8f6f4 v[68:71], v[2:9], v[34:41], v[68:71], v1, v246 op_sel_hi:[0,0,0]
	v_med3_f32 v122, v122, s30, v227
	v_med3_f32 v82, v82, s30, v227
	v_med3_f32 v123, v123, s30, v227
	v_med3_f32 v83, v83, s30, v227
	s_setprio 0
	s_branch .LBB0_1070
.Lg2c_nf1:
	v_med3_f32 v172, v172, s30, v227
	v_med3_f32 v176, v176, s30, v227
	v_med3_f32 v173, v173, s30, v227
	v_med3_f32 v177, v177, s30, v227
	v_med3_f32 v174, v174, s30, v227
	v_med3_f32 v178, v178, s30, v227
	v_med3_f32 v175, v175, s30, v227
	v_med3_f32 v179, v179, s30, v227
	v_med3_f32 v188, v188, s30, v227
	v_med3_f32 v192, v192, s30, v227
	v_med3_f32 v189, v189, s30, v227
	v_med3_f32 v193, v193, s30, v227
	v_med3_f32 v190, v190, s30, v227
	v_med3_f32 v194, v194, s30, v227
	v_med3_f32 v191, v191, s30, v227
	v_med3_f32 v195, v195, s30, v227
	v_med3_f32 v168, v168, s30, v227
	v_med3_f32 v164, v164, s30, v227
	v_med3_f32 v169, v169, s30, v227
	v_med3_f32 v165, v165, s30, v227
	v_med3_f32 v170, v170, s30, v227
	v_med3_f32 v166, v166, s30, v227
	v_med3_f32 v171, v171, s30, v227
	v_med3_f32 v167, v167, s30, v227
	v_med3_f32 v184, v184, s30, v227
	v_med3_f32 v180, v180, s30, v227
	v_med3_f32 v185, v185, s30, v227
	v_med3_f32 v181, v181, s30, v227
	v_med3_f32 v186, v186, s30, v227
	v_med3_f32 v182, v182, s30, v227
	v_med3_f32 v187, v187, s30, v227
	v_med3_f32 v183, v183, s30, v227
	v_med3_f32 v136, v136, s30, v227
	v_med3_f32 v137, v137, s30, v227
	v_med3_f32 v144, v144, s30, v227
	v_med3_f32 v145, v145, s30, v227
	v_med3_f32 v138, v138, s30, v227
	v_med3_f32 v139, v139, s30, v227
	v_med3_f32 v148, v148, s30, v227
	v_med3_f32 v149, v149, s30, v227
	v_med3_f32 v152, v152, s30, v227
	v_med3_f32 v153, v153, s30, v227
	v_med3_f32 v150, v150, s30, v227
	v_med3_f32 v151, v151, s30, v227
	v_med3_f32 v112, v112, s30, v227
	v_med3_f32 v113, v113, s30, v227
	v_med3_f32 v116, v116, s30, v227
	v_med3_f32 v117, v117, s30, v227
	v_med3_f32 v146, v146, s30, v227
	v_med3_f32 v147, v147, s30, v227
	v_med3_f32 v114, v114, s30, v227
	v_med3_f32 v115, v115, s30, v227
	v_med3_f32 v154, v154, s30, v227
	v_med3_f32 v155, v155, s30, v227
	v_med3_f32 v120, v120, s30, v227
	v_med3_f32 v80, v80, s30, v227
	v_med3_f32 v121, v121, s30, v227
	v_med3_f32 v81, v81, s30, v227
	v_med3_f32 v118, v118, s30, v227
	v_med3_f32 v119, v119, s30, v227
	v_med3_f32 v122, v122, s30, v227
	v_med3_f32 v82, v82, s30, v227
	v_med3_f32 v123, v123, s30, v227
	v_med3_f32 v83, v83, s30, v227

; #define LAS __attribute__((address_space(3)))
;     __device__ __forceinline__ u32x4 pack(const f32x4 (&acc)[2][2][4][2], int ai, int m) const {
;         u32x4 w;
; #pragma unroll
;         for (int bj = 0; bj < 2; ++bj) {
;             f32x4 v0 = acc[ai][bj][m][0], v1 = acc[ai][bj][m][1];
; #pragma unroll
;             for (int j = 0; j < 4; ++j) { v0[j] = fminf(fmaxf(v0[j], -448.f), 448.f); v1[j] = fminf(fmaxf(v1[j], -448.f), 448.f); }
;             int w0 = __builtin_amdgcn_cvt_pk_fp8_f32(v0[0], v0[1], 0, false); w0 = __builtin_amdgcn_cvt_pk_fp8_f32(v0[2], v0[3], w0, true);
;             int w1 = __builtin_amdgcn_cvt_pk_fp8_f32(v1[0], v1[1], 0, false); w1 = __builtin_amdgcn_cvt_pk_fp8_f32(v1[2], v1[3], w1, true);
;     __device__ __forceinline__ void operator()(const f32x4 (&acc)[2][2][4][2], const Unit& u, int wr, int wc, int fr, int fq) const {
;     ...
;         const int wofs = (32 * wr + fr) * 256 + (((4 * wc + fq) ^ fr) << 4);
;         const int rr0 = 8 * wv + (lane >> 4);
;         const int rofs = rr0 * 256 + (((lane & 15) ^ (rr0 & 15)) << 4), rofs4 = (rr0 + 4) * 256 + (((lane & 15) ^ ((rr0 + 4) & 15)) << 4);
;         const int t0 = 64 * (rr0 >> 5) + 16 * ((rr0 >> 4) & 1) + (rr0 & 15);
;         unsigned char* yp = Y + (size_t)u.row0 * D + u.nt * 256 + 16 * (lane & 15);
;         { const u32x4 wa = pack(acc, 0, 0), wb = pack(acc, 0, 1); *(LAS u32x4*)(lds + B0 + wofs) = wa; *(LAS u32x4*)(lds + B0 + wofs + 16 * 256) = wb; }
; #pragma unroll
;         for (int sl = 0; sl < 4; ++sl) { const int ai = sl >> 1, mh = sl & 1;
;             asm volatile("s_waitcnt lgkmcnt(0)" ::: "memory"); __builtin_amdgcn_s_barrier();
;             const int rb = (sl & 1) ? B1 : B0, wb_ = (sl & 1) ? B0 : B1;
;             const u32x4 v0 = *(const LAS u32x4*)(lds + rb + rofs), v1 = *(const LAS u32x4*)(lds + rb + rofs4);
;             if (sl < 3) { const int a2 = (sl + 1) >> 1, m2 = ((sl + 1) & 1) * 2;
;                 const u32x4 wa = pack(acc, a2, m2), wb = pack(acc, a2, m2 + 1); *(LAS u32x4*)(lds + wb_ + wofs) = wa; *(LAS u32x4*)(lds + wb_ + wofs + 16 * 256) = wb; }
;             const int rl = ai * 128 + mh * 32 + t0;
;             if (!nost) { if (rl < u.nv) __builtin_nontemporal_store(v0, (u32x4*)(yp + (size_t)rl * D)); if (rl + 4 < u.nv) __builtin_nontemporal_store(v1, (u32x4*)(yp + (size_t)(rl + 4) * D)); } }
.LBB0_1072:
	v_cvt_pk_fp8_f32 v2, v172, v173
	v_cvt_pk_fp8_f32 v3, v176, v177
	v_cvt_pk_fp8_f32 v2, v174, v175 op_sel:[0,0,1]
	v_cvt_pk_fp8_f32 v3, v178, v179 op_sel:[0,0,1]
	v_cvt_pk_fp8_f32 v4, v188, v189
	v_cvt_pk_fp8_f32 v5, v192, v193
	v_cvt_pk_fp8_f32 v4, v190, v191 op_sel:[0,0,1]
	v_cvt_pk_fp8_f32 v5, v194, v195 op_sel:[0,0,1]
	v_cvt_pk_fp8_f32 v6, v168, v169
	v_cvt_pk_fp8_f32 v7, v164, v165
	v_cvt_pk_fp8_f32 v6, v170, v171 op_sel:[0,0,1]
	v_cvt_pk_fp8_f32 v7, v166, v167 op_sel:[0,0,1]
	v_cvt_pk_fp8_f32 v8, v184, v185
	v_cvt_pk_fp8_f32 v9, v180, v181
	v_cvt_pk_fp8_f32 v8, v186, v187 op_sel:[0,0,1]
	v_cvt_pk_fp8_f32 v9, v182, v183 op_sel:[0,0,1]
	s_nop 15
	s_nop 15
	ds_write_b128 v207, v[2:5] offset:49152
	ds_write_b128 v207, v[6:9] offset:53248
	v_cvt_pk_fp8_f32 v15, v136, v137
	v_mov_b32_e32 v14, 0
	v_cvt_pk_fp8_f32 v14, v144, v145
	v_cvt_pk_fp8_f32 v15, v138, v139 op_sel:[0,0,1]
	v_cvt_pk_fp8_f32 v17, v148, v149
	v_mov_b32_e32 v16, 0
	v_cvt_pk_fp8_f32 v16, v152, v153
	v_cvt_pk_fp8_f32 v17, v150, v151 op_sel:[0,0,1]
	v_cvt_pk_fp8_f32 v19, v112, v113
	v_cvt_pk_fp8_f32 v18, v116, v117
	v_cvt_pk_fp8_f32 v14, v146, v147 op_sel:[0,0,1]
	v_cvt_pk_fp8_f32 v19, v114, v115 op_sel:[0,0,1]
	v_cvt_pk_fp8_f32 v16, v154, v155 op_sel:[0,0,1]
	v_cvt_pk_fp8_f32 v20, v120, v121
	v_cvt_pk_fp8_f32 v21, v80, v81
	s_ashr_i32 s87, s86, 31
	s_lshl_b64 s[4:5], s[86:87], 10
	v_cvt_pk_fp8_f32 v18, v118, v119 op_sel:[0,0,1]
	s_add_u32 s4, s17, s4
	s_addc_u32 s5, s20, s5
	s_lshl_b32 s18, s34, 8
	s_waitcnt lgkmcnt(0)
	s_barrier
	v_cvt_pk_fp8_f32 v20, v122, v123 op_sel:[0,0,1]
	v_cvt_pk_fp8_f32 v21, v82, v83 op_sel:[0,0,1]
	ds_read_b128 v[6:9], v231 offset:49152
	ds_read_b128 v[2:5], v235 offset:49152
	s_ashr_i32 s19, s18, 31
	s_add_u32 s4, s4, s18
	s_addc_u32 s5, s5, s19
	v_lshl_add_u64 v[10:11], s[4:5], 0, v[204:205]
	v_add_u32_e32 v12, 0x20410, v207
	v_cmp_gt_i32_e32 vcc, s6, v206
	ds_write_b128 v12, v[14:17]
	ds_write_b128 v211, v[18:21]
	s_and_saveexec_b64 s[4:5], vcc
	s_cbranch_execz .LBB0_1074
	v_lshl_add_u64 v[14:15], v[10:11], 0, v[208:209]
	s_waitcnt lgkmcnt(0)
	global_store_dwordx4 v[14:15], v[6:9], off nt
